# baseline (speedup 1.0000x reference)
_Z14seg_sum_kernelPKfS0_S0_PDv8_DF16bS2_Pf:
	s_ashr_i32 s4, s2, 2
	s_load_dwordx4 s[12:15], s[0:1], 0x0
	s_and_b32 s3, s2, 7
	s_and_b32 s4, s4, -8
	s_or_b32 s3, s4, s3
	v_readfirstlane_b32 s5, v0
	s_ashr_i32 s4, s3, 2
	s_lshr_b32 s11, s5, 6
	s_mul_hi_u32 s5, s5, 0xaaaaaaab
	s_lshr_b32 s23, s5, 7
	s_ashr_i32 s5, s4, 31
	s_and_b32 s22, s2, 3
	s_lshl_b64 s[6:7], s[4:5], 19
	s_waitcnt lgkmcnt(0)
	s_cmp_lg_u32 s11, 0
	s_cbranch_scc1 .Lno_touch
	s_mul_i32 s36, s3, 0x300000
	s_add_u32 s38, s12, s36
	s_addc_u32 s39, s13, 0
	s_movk_i32 s37, 0x6000
	v_mul_u32_u24_e32 v138, s37, v0
	v_lshlrev_b32_e32 v138, 1, v138
	global_load_dword v139, v138, s[38:39] nt
.Lno_touch:
	s_add_u32 s5, s14, s6
	s_addc_u32 s6, s15, s7
	s_lshl_b32 s14, s22, 10
	s_lshl_b32 s8, s22, 12
	s_add_u32 s8, s5, s8
	v_lshlrev_b32_e32 v2, 6, v0
	v_add_u32_e32 v122, 0x300, v0
	s_addc_u32 s9, s6, 0
	v_lshlrev_b32_e32 v1, 4, v0
	v_and_b32_e32 v2, 0xc000, v2
	v_mov_b32_e32 v3, 0
	v_lshlrev_b32_e32 v6, 6, v122
	v_lshl_add_u64 v[4:5], s[8:9], 0, v[2:3]
	v_and_b32_e32 v2, 0xff0, v1
	v_lshlrev_b32_e32 v1, 4, v122
	v_and_b32_e32 v6, 0x1c000, v6
	v_mov_b32_e32 v7, v3
	v_lshl_add_u64 v[4:5], v[4:5], 0, v[2:3]
	v_lshl_add_u64 v[6:7], s[8:9], 0, v[6:7]
	v_and_b32_e32 v8, 0xff0, v1
	v_mov_b32_e32 v9, v3
	v_add_u32_e32 v123, 0x600, v0
	v_lshl_add_u64 v[6:7], v[6:7], 0, v[8:9]
	global_load_dwordx4 v[82:85], v[4:5], off nt
	global_load_dwordx4 v[78:81], v[6:7], off nt
	v_lshlrev_b32_e32 v4, 6, v123
	v_lshlrev_b32_e32 v1, 4, v123
	v_and_b32_e32 v4, 0x3c000, v4
	v_mov_b32_e32 v5, v3
	v_lshl_add_u64 v[4:5], s[8:9], 0, v[4:5]
	v_and_b32_e32 v6, 0xff0, v1
	v_mov_b32_e32 v7, v3
	v_add_u32_e32 v124, 0x900, v0
	v_lshl_add_u64 v[4:5], v[4:5], 0, v[6:7]
	v_lshlrev_b32_e32 v6, 6, v124
	v_lshlrev_b32_e32 v1, 4, v124
	v_and_b32_e32 v6, 0x3c000, v6
	v_lshl_add_u64 v[6:7], s[8:9], 0, v[6:7]
	v_and_b32_e32 v8, 0xff0, v1
	v_or_b32_e32 v125, 0xc00, v0
	v_lshl_add_u64 v[6:7], v[6:7], 0, v[8:9]
	v_lshlrev_b32_e32 v1, 6, v125
	v_add_u32_e32 v130, 0xf00, v0
	global_load_dwordx4 v[90:93], v[4:5], off nt
	global_load_dwordx4 v[86:89], v[6:7], off nt
	v_and_b32_e32 v4, 0x3c000, v1
	v_mov_b32_e32 v5, v3
	v_lshlrev_b32_e32 v6, 6, v130
	v_lshl_add_u64 v[4:5], s[8:9], 0, v[4:5]
	v_lshlrev_b32_e32 v1, 4, v130
	v_and_b32_e32 v6, 0x7c000, v6
	v_mov_b32_e32 v7, v3
	v_lshl_add_u64 v[4:5], v[4:5], 0, v[2:3]
	v_lshl_add_u64 v[6:7], s[8:9], 0, v[6:7]
	v_and_b32_e32 v8, 0xff0, v1
	v_add_u32_e32 v131, 0x1200, v0
	v_lshl_add_u64 v[6:7], v[6:7], 0, v[8:9]
	global_load_dwordx4 v[98:101], v[4:5], off nt
	global_load_dwordx4 v[94:97], v[6:7], off nt
	v_lshlrev_b32_e32 v4, 6, v131
	v_lshlrev_b32_e32 v1, 4, v131
	v_and_b32_e32 v4, 0x5c000, v4
	v_mov_b32_e32 v5, v3
	v_lshl_add_u64 v[4:5], s[8:9], 0, v[4:5]
	v_and_b32_e32 v6, 0xff0, v1
	v_mov_b32_e32 v7, v3
	v_add_u32_e32 v134, 0x1500, v0
	v_lshl_add_u64 v[4:5], v[4:5], 0, v[6:7]
	v_lshlrev_b32_e32 v6, 6, v134
	v_lshlrev_b32_e32 v1, 4, v134
	v_and_b32_e32 v6, 0x7c000, v6
	v_or_b32_e32 v135, 0x1800, v0
	v_lshl_add_u64 v[6:7], s[8:9], 0, v[6:7]
	v_and_b32_e32 v8, 0xff0, v1
	v_lshlrev_b32_e32 v1, 6, v135
	v_lshl_add_u64 v[6:7], v[6:7], 0, v[8:9]
	global_load_dwordx4 v[106:109], v[4:5], off nt
	global_load_dwordx4 v[102:105], v[6:7], off nt
	v_and_b32_e32 v4, 0x6c000, v1
	v_mov_b32_e32 v5, v3
	v_lshl_add_u64 v[4:5], s[8:9], 0, v[4:5]
	v_add_u32_e32 v136, 0x1b00, v0
	v_lshl_add_u64 v[4:5], v[4:5], 0, v[2:3]
	v_lshlrev_b32_e32 v2, 6, v136
	v_lshlrev_b32_e32 v1, 4, v136
	v_and_b32_e32 v2, 0x7c000, v2
	v_lshl_add_u64 v[6:7], s[8:9], 0, v[2:3]
	v_and_b32_e32 v2, 0xff0, v1
	v_add_u32_e32 v137, 0x1e00, v0
	v_lshl_add_u64 v[6:7], v[6:7], 0, v[2:3]
	v_min_u32_e32 v1, 0x1fff, v137
	global_load_dwordx4 v[118:121], v[4:5], off nt
	global_load_dwordx4 v[110:113], v[6:7], off nt
	v_lshlrev_b32_e32 v6, 4, v1
	v_lshlrev_b32_e32 v1, 6, v1
	v_and_b32_e32 v2, 0x7c000, v1
	v_bfe_u32 v127, v0, 4, 2
	s_lshl_b32 s4, s4, 12
	v_lshl_add_u64 v[4:5], s[8:9], 0, v[2:3]
	v_and_b32_e32 v2, 0xff0, v6
	v_lshlrev_b32_e32 v133, 3, v127
	s_or_b32 s4, s14, s4
	v_lshl_add_u64 v[4:5], v[4:5], 0, v[2:3]
	s_lshl_b32 s26, s23, 8
	v_or_b32_e32 v2, s4, v133
	s_movk_i32 s10, 0xc00
	global_load_dwordx4 v[114:117], v[4:5], off nt
	s_mul_hi_u32 s6, s11, 0x55555556
	v_add_u32_e32 v28, s26, v2
	v_mov_b64_e32 v[4:5], s[12:13]
	s_mov_b32 s7, 0
	s_bfe_u32 s24, s2, 0x20003
	s_mul_i32 s6, s6, 3
	v_mad_i64_i32 v[4:5], s[8:9], v28, s10, v[4:5]
	s_sub_i32 s25, s11, s6
	s_mul_i32 s8, s24, 0x300
	s_mov_b32 s9, s7
	v_and_b32_e32 v1, 15, v0
	v_lshl_add_u64 v[4:5], v[4:5], 0, s[8:9]
	s_lshl_b32 s8, s25, 8
	v_lshl_add_u64 v[4:5], v[4:5], 0, s[8:9]
	v_lshlrev_b32_e32 v2, 4, v1
	v_lshl_add_u64 v[4:5], v[4:5], 0, v[2:3]
	s_movk_i32 s4, 0x1000
	v_add_co_u32_e32 v6, vcc, s4, v4
	s_movk_i32 s4, 0x2000
	s_nop 0
	v_addc_co_u32_e32 v7, vcc, 0, v5, vcc
	v_add_co_u32_e32 v8, vcc, s4, v4
	s_movk_i32 s4, 0x3000
	s_nop 0
	v_addc_co_u32_e32 v9, vcc, 0, v5, vcc
	global_load_dwordx4 v[18:21], v[4:5], off nt
	global_load_dwordx4 v[30:33], v[4:5], off offset:3072 nt
	global_load_dwordx4 v[46:49], v[6:7], off offset:2048 nt
	global_load_dwordx4 v[50:53], v[8:9], off offset:1024 nt
	v_add_co_u32_e32 v6, vcc, s4, v4
	s_movk_i32 s4, 0x4000
	s_nop 0
	v_addc_co_u32_e32 v7, vcc, 0, v5, vcc
	global_load_dwordx4 v[62:65], v[6:7], off nt
	global_load_dwordx4 v[66:69], v[6:7], off offset:3072 nt
	v_add_co_u32_e32 v6, vcc, s4, v4
	s_movk_i32 s4, 0x5000
	s_nop 0
	v_addc_co_u32_e32 v7, vcc, 0, v5, vcc
	v_add_co_u32_e32 v8, vcc, s4, v4
	s_mov_b32 s4, 0x18000
	s_nop 0
	v_addc_co_u32_e32 v9, vcc, 0, v5, vcc
	v_add_co_u32_e32 v10, vcc, s4, v4
	s_mov_b32 s4, 0x19000
	s_nop 0
	v_addc_co_u32_e32 v11, vcc, 0, v5, vcc
	v_add_co_u32_e32 v14, vcc, s4, v4
	s_mov_b32 s4, 0x1a000
	s_nop 0
	v_addc_co_u32_e32 v15, vcc, 0, v5, vcc
	v_add_co_u32_e32 v22, vcc, s4, v4
	s_mov_b32 s4, 0x1b000
	s_nop 0
	v_addc_co_u32_e32 v23, vcc, 0, v5, vcc
	v_add_co_u32_e32 v26, vcc, s4, v4
	s_mov_b32 s5, 0x1c000
	s_nop 0
	v_addc_co_u32_e32 v27, vcc, 0, v5, vcc
	global_load_dwordx4 v[70:73], v[6:7], off offset:2048 nt
	global_load_dwordx4 v[74:77], v[8:9], off offset:1024 nt
	s_nop 0
	global_load_dwordx4 v[6:9], v[10:11], off nt
	s_nop 0
	global_load_dwordx4 v[10:13], v[10:11], off offset:3072 nt
	s_nop 0
	global_load_dwordx4 v[14:17], v[14:15], off offset:2048 nt
	s_nop 0
	global_load_dwordx4 v[22:25], v[22:23], off offset:1024 nt
	s_nop 0
	global_load_dwordx4 v[38:41], v[26:27], off nt
	global_load_dwordx4 v[42:45], v[26:27], off offset:3072 nt
	v_add_co_u32_e32 v26, vcc, s5, v4
	s_mov_b32 s4, 0x1d000
	s_nop 0
	v_addc_co_u32_e32 v27, vcc, 0, v5, vcc
	v_add_co_u32_e32 v4, vcc, s4, v4
	v_lshrrev_b32_e32 v126, 3, v0
	s_nop 0
	v_addc_co_u32_e32 v5, vcc, 0, v5, vcc
	global_load_dwordx4 v[54:57], v[26:27], off offset:2048 nt
	global_load_dwordx4 v[58:61], v[4:5], off offset:1024 nt
	v_mad_i64_i32 v[4:5], s[4:5], v28, s10, 0
	s_lshl_b32 s4, s2, 1
	s_nop 0
	v_bfi_b32 v132, -8, s4, v0
	v_mad_u64_u32 v[128:129], s[4:5], s22, 24, v[126:127]
	s_movk_i32 s4, 0xc0
	s_lshl_b32 s6, s25, 6
	v_cmp_gt_u32_e64 s[4:5], s4, v0
	v_mov_b32_e32 v26, v3
	v_mov_b32_e32 v27, v3
	v_mov_b32_e32 v28, v3
	v_mov_b32_e32 v29, v3
	v_mov_b32_e32 v34, v3
	v_mov_b32_e32 v35, v3
	v_mov_b32_e32 v36, v3
	v_mov_b32_e32 v37, v3
	s_and_saveexec_b64 s[8:9], s[4:5]
	s_cbranch_execz .LBB0_2
	s_load_dwordx2 s[14:15], s[0:1], 0x10
	v_lshlrev_b32_e32 v26, 5, v128
	v_mov_b32_e32 v27, 0
	s_waitcnt lgkmcnt(0)
	v_mov_b64_e32 v[28:29], s[14:15]
	v_mad_i64_i32 v[28:29], s[10:11], v132, s10, v[28:29]
	v_lshl_add_u64 v[34:35], v[28:29], 0, v[26:27]
	global_load_dwordx4 v[26:29], v[34:35], off offset:16
	s_nop 0
	global_load_dwordx4 v[34:37], v[34:35], off
